# MoE stream loops: X-row wait/LDS write/next request moved to the end of the half-step, so the in-order vmcnt wait no longer retires the in-flight weight tile early
# baseline (speedup 1.0000x reference)
.LBB0_1720:
	s_add_i32 s0, s0, 2
	s_min_u32 s1, s0, 28
	s_lshl_b32 s12, s1, 17
	s_add_i32 s12, s12, 0x60000
	s_add_i32 s58, s85, 0x20000
	s_cmp_gt_u32 s0, 28
	s_cselect_b32 s12, s58, s12
	s_waitcnt vmcnt(12)
	v_cvt_pk_bf16_f32 v164, v74, v78
	s_waitcnt vmcnt(10)
	v_cvt_pk_bf16_f32 v165, v82, v86
	v_cvt_pk_bf16_f32 v166, v75, v79
	v_cvt_pk_bf16_f32 v167, v83, v87
	v_cvt_pk_bf16_f32 v190, v76, v80
	v_cvt_pk_bf16_f32 v191, v84, v88
	v_cvt_pk_bf16_f32 v192, v77, v81
	v_cvt_pk_bf16_f32 v193, v85, v89
	buffer_load_dwordx4 v[74:77], v160, s[8:11], s12 offen nt
	buffer_load_dwordx4 v[78:81], v90, s[8:11], s12 offen nt
	buffer_load_dwordx4 v[82:85], v178, s[8:11], s12 offen nt
	buffer_load_dwordx4 v[86:89], v179, s[8:11], s12 offen nt
	v_add_u32_e32 v194, 0x4000, v188
	v_add_u32_e32 v195, 0x4000, v180
	v_add_u32_e32 v214, v173, v174
	ds_write2_b64 v194, v[164:165], v[166:167] offset1:16
	ds_write2_b64 v195, v[190:191], v[192:193] offset0:32 offset1:48
	v_add_u32_e32 v215, v176, v174
	ds_read_b128 v[164:167], v214 offset:32768
	ds_read_b128 v[190:193], v214 offset:34816
	ds_read_b128 v[194:197], v214 offset:36864
	ds_read_b128 v[198:201], v215
	ds_read_b128 v[202:205], v215 offset:2048
	ds_read_b128 v[206:209], v215 offset:4096
	ds_read_b128 v[210:213], v215 offset:6144
	s_waitcnt lgkmcnt(3)
	v_mfma_f32_16x16x32_bf16 v[152:155], v[198:201], v[164:167], v[152:155]
	v_mfma_f32_16x16x32_bf16 v[62:65], v[198:201], v[190:193], v[62:65]
	v_mfma_f32_16x16x32_bf16 v[30:33], v[198:201], v[194:197], v[30:33]
	s_waitcnt lgkmcnt(2)
	v_mfma_f32_16x16x32_bf16 v[120:123], v[202:205], v[164:167], v[120:123]
	v_mfma_f32_16x16x32_bf16 v[54:57], v[202:205], v[190:193], v[54:57]
	v_mfma_f32_16x16x32_bf16 v[22:25], v[202:205], v[194:197], v[22:25]
	s_waitcnt lgkmcnt(1)
	v_mfma_f32_16x16x32_bf16 v[112:115], v[206:209], v[164:167], v[112:115]
	v_mfma_f32_16x16x32_bf16 v[46:49], v[206:209], v[190:193], v[46:49]
	v_mfma_f32_16x16x32_bf16 v[14:17], v[206:209], v[194:197], v[14:17]
	s_waitcnt lgkmcnt(0)
	v_mfma_f32_16x16x32_bf16 v[70:73], v[210:213], v[164:167], v[70:73]
	v_mfma_f32_16x16x32_bf16 v[38:41], v[210:213], v[190:193], v[38:41]
	v_mfma_f32_16x16x32_bf16 v[6:9], v[210:213], v[194:197], v[6:9]
	ds_read_b128 v[198:201], v215 offset:8192
	ds_read_b128 v[202:205], v215 offset:10240
	ds_read_b128 v[206:209], v215 offset:12288
	ds_read_b128 v[210:213], v215 offset:14336
	s_waitcnt lgkmcnt(3)
	v_mfma_f32_16x16x32_bf16 v[148:151], v[198:201], v[164:167], v[148:151]
	v_mfma_f32_16x16x32_bf16 v[58:61], v[198:201], v[190:193], v[58:61]
	v_mfma_f32_16x16x32_bf16 v[26:29], v[198:201], v[194:197], v[26:29]
	s_waitcnt lgkmcnt(2)
	v_mfma_f32_16x16x32_bf16 v[116:119], v[202:205], v[164:167], v[116:119]
	v_mfma_f32_16x16x32_bf16 v[50:53], v[202:205], v[190:193], v[50:53]
	v_mfma_f32_16x16x32_bf16 v[18:21], v[202:205], v[194:197], v[18:21]
	s_waitcnt lgkmcnt(1)
	v_mfma_f32_16x16x32_bf16 v[92:95], v[206:209], v[164:167], v[92:95]
	v_mfma_f32_16x16x32_bf16 v[42:45], v[206:209], v[190:193], v[42:45]
	v_mfma_f32_16x16x32_bf16 v[10:13], v[206:209], v[194:197], v[10:13]
	s_waitcnt lgkmcnt(0)
	v_mfma_f32_16x16x32_bf16 v[66:69], v[210:213], v[164:167], v[66:69]
	v_mfma_f32_16x16x32_bf16 v[34:37], v[210:213], v[190:193], v[34:37]
	v_mfma_f32_16x16x32_bf16 v[2:5], v[210:213], v[194:197], v[2:5]
	v_add_u32_e32 v216, v173, v175
	ds_read_b128 v[164:167], v216 offset:32768
	ds_read_b128 v[190:193], v216 offset:34816
	v_add_u32_e32 v217, v176, v175
	ds_read_b128 v[194:197], v216 offset:36864
	ds_read_b128 v[198:201], v217
	ds_read_b128 v[202:205], v217 offset:2048
	ds_read_b128 v[206:209], v217 offset:4096
	ds_read_b128 v[210:213], v217 offset:6144
	s_waitcnt lgkmcnt(3)
	v_mfma_f32_16x16x32_bf16 v[152:155], v[198:201], v[164:167], v[152:155]
	v_mfma_f32_16x16x32_bf16 v[62:65], v[198:201], v[190:193], v[62:65]
	v_mfma_f32_16x16x32_bf16 v[30:33], v[198:201], v[194:197], v[30:33]
	s_waitcnt lgkmcnt(2)
	v_mfma_f32_16x16x32_bf16 v[120:123], v[202:205], v[164:167], v[120:123]
	v_mfma_f32_16x16x32_bf16 v[54:57], v[202:205], v[190:193], v[54:57]
	v_mfma_f32_16x16x32_bf16 v[22:25], v[202:205], v[194:197], v[22:25]
	s_waitcnt lgkmcnt(1)
	v_mfma_f32_16x16x32_bf16 v[112:115], v[206:209], v[164:167], v[112:115]
	v_mfma_f32_16x16x32_bf16 v[46:49], v[206:209], v[190:193], v[46:49]
	v_mfma_f32_16x16x32_bf16 v[14:17], v[206:209], v[194:197], v[14:17]
	s_waitcnt lgkmcnt(0)
	v_mfma_f32_16x16x32_bf16 v[70:73], v[210:213], v[164:167], v[70:73]
	v_mfma_f32_16x16x32_bf16 v[38:41], v[210:213], v[190:193], v[38:41]
	v_mfma_f32_16x16x32_bf16 v[6:9], v[210:213], v[194:197], v[6:9]
	ds_read_b128 v[198:201], v217 offset:8192
	ds_read_b128 v[202:205], v217 offset:10240
	ds_read_b128 v[206:209], v217 offset:12288
	ds_read_b128 v[210:213], v217 offset:14336
	s_waitcnt lgkmcnt(3)
	v_mfma_f32_16x16x32_bf16 v[148:151], v[198:201], v[164:167], v[148:151]
	s_min_u32 s12, s0, 27
	s_waitcnt lgkmcnt(0)
	v_mfma_f32_16x16x32_bf16 v[116:119], v[202:205], v[164:167], v[116:119]
	s_barrier
	s_lshl_b32 s12, s12, 17
	v_mfma_f32_16x16x32_bf16 v[92:95], v[206:209], v[164:167], v[92:95]
	s_add_i32 s12, s12, 0x80000
	s_sub_i32 s58, s0, 28
	s_lshl_b32 s58, s58, 17
	s_add_i32 s58, s58, s85
	s_cmp_gt_u32 s0, 27
	s_cselect_b32 s12, s58, s12
	v_mfma_f32_16x16x32_bf16 v[66:69], v[210:213], v[164:167], v[66:69]
	s_min_u32 s43, s0, 29
	s_lshl_b32 s43, s43, 7
	s_waitcnt vmcnt(9)
	ds_write_b128 v189, v[132:135] offset:38912
	s_waitcnt vmcnt(8)
	ds_write_b128 v181, v[124:127] offset:39936
	s_waitcnt vmcnt(7)
	ds_write_b128 v189, v[140:143] offset:40960
	s_waitcnt vmcnt(6)
	ds_write_b128 v181, v[144:147] offset:41984
	s_waitcnt vmcnt(5)
	ds_write_b128 v189, v[128:131] offset:43008
	s_waitcnt vmcnt(4)
	ds_write_b128 v181, v[136:139] offset:44032
	s_addk_i32 s43, 0x100
	s_cmp_lt_u32 s0, 30
	s_cbranch_scc1 .Lxk_nx0
	s_cmp_eq_u32 s84, 0
	s_cbranch_scc1 .Lxk_nx0
	s_mov_b32 s43, 0
	v_lshl_or_b32 v182, v246, 12, v163
	v_lshl_or_b32 v183, v247, 12, v163
	v_lshl_or_b32 v184, v248, 12, v163
	v_lshl_or_b32 v185, v249, 12, v163
	v_lshl_or_b32 v186, v250, 12, v163
	v_lshl_or_b32 v187, v251, 12, v163
.Lxk_nx0:
	buffer_load_dwordx4 v[124:127], v182, s[4:7], s43 offen
	buffer_load_dwordx4 v[128:131], v183, s[4:7], s43 offen
	buffer_load_dwordx4 v[132:135], v184, s[4:7], s43 offen
	buffer_load_dwordx4 v[136:139], v185, s[4:7], s43 offen
	buffer_load_dwordx4 v[140:143], v186, s[4:7], s43 offen
	buffer_load_dwordx4 v[144:147], v187, s[4:7], s43 offen
	v_cvt_pk_bf16_f32 v164, v96, v100
	v_cvt_pk_bf16_f32 v165, v104, v108
	v_cvt_pk_bf16_f32 v96, v97, v101
	v_cvt_pk_bf16_f32 v97, v105, v109
	ds_write2_b64 v188, v[164:165], v[96:97] offset1:16
	v_cvt_pk_bf16_f32 v96, v98, v102
	v_cvt_pk_bf16_f32 v97, v106, v110
	v_cvt_pk_bf16_f32 v98, v99, v103
	v_cvt_pk_bf16_f32 v99, v107, v111
	ds_write2_b64 v180, v[96:97], v[98:99] offset0:32 offset1:48
	buffer_load_dwordx4 v[96:99], v160, s[8:11], s12 offen nt
	buffer_load_dwordx4 v[100:103], v90, s[8:11], s12 offen nt
	buffer_load_dwordx4 v[104:107], v178, s[8:11], s12 offen nt
	buffer_load_dwordx4 v[108:111], v179, s[8:11], s12 offen nt
	v_mfma_f32_16x16x32_bf16 v[58:61], v[198:201], v[190:193], v[58:61]
	v_mfma_f32_16x16x32_bf16 v[26:29], v[198:201], v[194:197], v[26:29]
	v_mfma_f32_16x16x32_bf16 v[50:53], v[202:205], v[190:193], v[50:53]
	v_mfma_f32_16x16x32_bf16 v[18:21], v[202:205], v[194:197], v[18:21]
	v_mfma_f32_16x16x32_bf16 v[42:45], v[206:209], v[190:193], v[42:45]
	v_mfma_f32_16x16x32_bf16 v[10:13], v[206:209], v[194:197], v[10:13]
	v_mfma_f32_16x16x32_bf16 v[34:37], v[210:213], v[190:193], v[34:37]
	v_mfma_f32_16x16x32_bf16 v[2:5], v[210:213], v[194:197], v[2:5]
	ds_read_b128 v[164:167], v214 offset:38912
	ds_read_b128 v[190:193], v214 offset:40960
	ds_read_b128 v[194:197], v214 offset:43008
	ds_read_b128 v[198:201], v215 offset:16384
	ds_read_b128 v[202:205], v215 offset:18432
	ds_read_b128 v[206:209], v215 offset:20480
	ds_read_b128 v[210:213], v215 offset:22528
	s_waitcnt lgkmcnt(3)
	v_mfma_f32_16x16x32_bf16 v[152:155], v[198:201], v[164:167], v[152:155]
	v_mfma_f32_16x16x32_bf16 v[62:65], v[198:201], v[190:193], v[62:65]
	v_mfma_f32_16x16x32_bf16 v[30:33], v[198:201], v[194:197], v[30:33]
	s_waitcnt lgkmcnt(2)
	v_mfma_f32_16x16x32_bf16 v[120:123], v[202:205], v[164:167], v[120:123]
	v_mfma_f32_16x16x32_bf16 v[54:57], v[202:205], v[190:193], v[54:57]
	v_mfma_f32_16x16x32_bf16 v[22:25], v[202:205], v[194:197], v[22:25]
	s_waitcnt lgkmcnt(1)
	v_mfma_f32_16x16x32_bf16 v[112:115], v[206:209], v[164:167], v[112:115]
	v_mfma_f32_16x16x32_bf16 v[46:49], v[206:209], v[190:193], v[46:49]
	v_mfma_f32_16x16x32_bf16 v[14:17], v[206:209], v[194:197], v[14:17]
	s_waitcnt lgkmcnt(0)
	v_mfma_f32_16x16x32_bf16 v[70:73], v[210:213], v[164:167], v[70:73]
	v_mfma_f32_16x16x32_bf16 v[38:41], v[210:213], v[190:193], v[38:41]
	v_mfma_f32_16x16x32_bf16 v[6:9], v[210:213], v[194:197], v[6:9]
	ds_read_b128 v[198:201], v215 offset:24576
	ds_read_b128 v[202:205], v215 offset:26624
	ds_read_b128 v[206:209], v215 offset:28672
	ds_read_b128 v[210:213], v215 offset:30720
	s_waitcnt lgkmcnt(3)
	v_mfma_f32_16x16x32_bf16 v[148:151], v[198:201], v[164:167], v[148:151]
	v_mfma_f32_16x16x32_bf16 v[58:61], v[198:201], v[190:193], v[58:61]
	v_mfma_f32_16x16x32_bf16 v[26:29], v[198:201], v[194:197], v[26:29]
	s_waitcnt lgkmcnt(2)
	v_mfma_f32_16x16x32_bf16 v[116:119], v[202:205], v[164:167], v[116:119]
	v_mfma_f32_16x16x32_bf16 v[50:53], v[202:205], v[190:193], v[50:53]
	v_mfma_f32_16x16x32_bf16 v[18:21], v[202:205], v[194:197], v[18:21]
	s_waitcnt lgkmcnt(1)
	v_mfma_f32_16x16x32_bf16 v[92:95], v[206:209], v[164:167], v[92:95]
	v_mfma_f32_16x16x32_bf16 v[42:45], v[206:209], v[190:193], v[42:45]
	v_mfma_f32_16x16x32_bf16 v[10:13], v[206:209], v[194:197], v[10:13]
	s_waitcnt lgkmcnt(0)
	v_mfma_f32_16x16x32_bf16 v[66:69], v[210:213], v[164:167], v[66:69]
	v_mfma_f32_16x16x32_bf16 v[34:37], v[210:213], v[190:193], v[34:37]
	v_mfma_f32_16x16x32_bf16 v[2:5], v[210:213], v[194:197], v[2:5]
	ds_read_b128 v[164:167], v216 offset:38912
	ds_read_b128 v[190:193], v216 offset:40960
	ds_read_b128 v[194:197], v216 offset:43008
	ds_read_b128 v[198:201], v217 offset:16384
	ds_read_b128 v[202:205], v217 offset:18432
	ds_read_b128 v[206:209], v217 offset:20480
	ds_read_b128 v[210:213], v217 offset:22528
	s_waitcnt lgkmcnt(3)
	v_mfma_f32_16x16x32_bf16 v[152:155], v[198:201], v[164:167], v[152:155]
	v_mfma_f32_16x16x32_bf16 v[62:65], v[198:201], v[190:193], v[62:65]
	v_mfma_f32_16x16x32_bf16 v[30:33], v[198:201], v[194:197], v[30:33]
	s_waitcnt lgkmcnt(2)
	v_mfma_f32_16x16x32_bf16 v[120:123], v[202:205], v[164:167], v[120:123]
	v_mfma_f32_16x16x32_bf16 v[54:57], v[202:205], v[190:193], v[54:57]
	v_mfma_f32_16x16x32_bf16 v[22:25], v[202:205], v[194:197], v[22:25]
	s_waitcnt lgkmcnt(1)
	v_mfma_f32_16x16x32_bf16 v[112:115], v[206:209], v[164:167], v[112:115]
	v_mfma_f32_16x16x32_bf16 v[46:49], v[206:209], v[190:193], v[46:49]
	v_mfma_f32_16x16x32_bf16 v[14:17], v[206:209], v[194:197], v[14:17]
	s_waitcnt lgkmcnt(0)
	v_mfma_f32_16x16x32_bf16 v[70:73], v[210:213], v[164:167], v[70:73]
	v_mfma_f32_16x16x32_bf16 v[38:41], v[210:213], v[190:193], v[38:41]
	v_mfma_f32_16x16x32_bf16 v[6:9], v[210:213], v[194:197], v[6:9]
	ds_read_b128 v[198:201], v217 offset:24576
	ds_read_b128 v[202:205], v217 offset:26624
	ds_read_b128 v[206:209], v217 offset:28672
	ds_read_b128 v[210:213], v217 offset:30720
	s_waitcnt lgkmcnt(3)
	v_mfma_f32_16x16x32_bf16 v[148:151], v[198:201], v[164:167], v[148:151]
	s_waitcnt lgkmcnt(0)
	s_barrier
	v_mfma_f32_16x16x32_bf16 v[58:61], v[198:201], v[190:193], v[58:61]
	v_mfma_f32_16x16x32_bf16 v[26:29], v[198:201], v[194:197], v[26:29]
	v_mfma_f32_16x16x32_bf16 v[116:119], v[202:205], v[164:167], v[116:119]
	v_mfma_f32_16x16x32_bf16 v[50:53], v[202:205], v[190:193], v[50:53]
	v_mfma_f32_16x16x32_bf16 v[18:21], v[202:205], v[194:197], v[18:21]
	v_mfma_f32_16x16x32_bf16 v[92:95], v[206:209], v[164:167], v[92:95]
	v_mfma_f32_16x16x32_bf16 v[42:45], v[206:209], v[190:193], v[42:45]
	v_mfma_f32_16x16x32_bf16 v[10:13], v[206:209], v[194:197], v[10:13]
	v_mfma_f32_16x16x32_bf16 v[66:69], v[210:213], v[164:167], v[66:69]
	v_mfma_f32_16x16x32_bf16 v[34:37], v[210:213], v[190:193], v[34:37]
	v_mfma_f32_16x16x32_bf16 v[2:5], v[210:213], v[194:197], v[2:5]
	s_lshl_b32 s1, s1, 7
	s_waitcnt vmcnt(9)
	ds_write_b128 v189, v[124:127] offset:32768
	s_waitcnt vmcnt(8)
	ds_write_b128 v181, v[128:131] offset:33792
	s_waitcnt vmcnt(7)
	ds_write_b128 v189, v[132:135] offset:34816
	s_waitcnt vmcnt(6)
	ds_write_b128 v181, v[136:139] offset:35840
	s_waitcnt vmcnt(5)
	ds_write_b128 v189, v[140:143] offset:36864
	s_waitcnt vmcnt(4)
	ds_write_b128 v181, v[144:147] offset:37888
	s_addk_i32 s1, 0x180
	s_cmp_eq_u32 s0, 30
	s_cselect_b32 s58, s84, 0
	s_cmp_lg_u32 s58, 0
	s_cselect_b32 s1, 0x80, s1
	buffer_load_dwordx4 v[132:135], v182, s[4:7], s1 offen
	buffer_load_dwordx4 v[124:127], v183, s[4:7], s1 offen
	buffer_load_dwordx4 v[140:143], v184, s[4:7], s1 offen
	buffer_load_dwordx4 v[144:147], v185, s[4:7], s1 offen
	buffer_load_dwordx4 v[128:131], v186, s[4:7], s1 offen
	buffer_load_dwordx4 v[136:139], v187, s[4:7], s1 offen
	s_cmp_gt_u32 s0, 29
	s_cbranch_scc0 .LBB0_1720
	s_branch .Lmoe_k_done
.Lmoe_k_b:
	s_add_i32 s0, s0, 2
	s_min_u32 s1, s0, 28
	s_lshl_b32 s12, s1, 17
	s_add_i32 s12, s12, 0x60000
	s_add_i32 s58, s85, 0x20000
	s_cmp_gt_u32 s0, 28
	s_cselect_b32 s12, s58, s12
	s_waitcnt vmcnt(12)
	v_cvt_pk_bf16_f32 v164, v74, v78
	s_waitcnt vmcnt(10)
	v_cvt_pk_bf16_f32 v165, v82, v86
	v_cvt_pk_bf16_f32 v166, v75, v79
	v_cvt_pk_bf16_f32 v167, v83, v87
	v_cvt_pk_bf16_f32 v190, v76, v80
	v_cvt_pk_bf16_f32 v191, v84, v88
	v_cvt_pk_bf16_f32 v192, v77, v81
	v_cvt_pk_bf16_f32 v193, v85, v89
	buffer_load_dwordx4 v[74:77], v160, s[8:11], s12 offen nt
	buffer_load_dwordx4 v[78:81], v90, s[8:11], s12 offen nt
	buffer_load_dwordx4 v[82:85], v178, s[8:11], s12 offen nt
	buffer_load_dwordx4 v[86:89], v179, s[8:11], s12 offen nt
	v_add_u32_e32 v194, 0x4000, v188
	v_add_u32_e32 v195, 0x4000, v180
	v_add_u32_e32 v214, v173, v174
	ds_write2_b64 v194, v[164:165], v[166:167] offset1:16
	ds_write2_b64 v195, v[190:191], v[192:193] offset0:32 offset1:48
	v_add_u32_e32 v215, v176, v174
	ds_read_b128 v[164:167], v214 offset:32768
	ds_read_b128 v[190:193], v214 offset:34816
	ds_read_b128 v[198:201], v215
	ds_read_b128 v[202:205], v215 offset:2048
	ds_read_b128 v[206:209], v215 offset:4096
	ds_read_b128 v[210:213], v215 offset:6144
	s_waitcnt lgkmcnt(3)
	v_mfma_f32_16x16x32_bf16 v[152:155], v[198:201], v[164:167], v[152:155]
	v_mfma_f32_16x16x32_bf16 v[62:65], v[198:201], v[190:193], v[62:65]
	s_waitcnt lgkmcnt(2)
	v_mfma_f32_16x16x32_bf16 v[120:123], v[202:205], v[164:167], v[120:123]
	v_mfma_f32_16x16x32_bf16 v[54:57], v[202:205], v[190:193], v[54:57]
	s_waitcnt lgkmcnt(1)
	v_mfma_f32_16x16x32_bf16 v[112:115], v[206:209], v[164:167], v[112:115]
	v_mfma_f32_16x16x32_bf16 v[46:49], v[206:209], v[190:193], v[46:49]
	s_waitcnt lgkmcnt(0)
	v_mfma_f32_16x16x32_bf16 v[70:73], v[210:213], v[164:167], v[70:73]
	v_mfma_f32_16x16x32_bf16 v[38:41], v[210:213], v[190:193], v[38:41]
	ds_read_b128 v[198:201], v215 offset:8192
	ds_read_b128 v[202:205], v215 offset:10240
	ds_read_b128 v[206:209], v215 offset:12288
	ds_read_b128 v[210:213], v215 offset:14336
	s_waitcnt lgkmcnt(3)
	v_mfma_f32_16x16x32_bf16 v[148:151], v[198:201], v[164:167], v[148:151]
	v_mfma_f32_16x16x32_bf16 v[58:61], v[198:201], v[190:193], v[58:61]
	s_waitcnt lgkmcnt(2)
	v_mfma_f32_16x16x32_bf16 v[116:119], v[202:205], v[164:167], v[116:119]
	v_mfma_f32_16x16x32_bf16 v[50:53], v[202:205], v[190:193], v[50:53]
	s_waitcnt lgkmcnt(1)
	v_mfma_f32_16x16x32_bf16 v[92:95], v[206:209], v[164:167], v[92:95]
	v_mfma_f32_16x16x32_bf16 v[42:45], v[206:209], v[190:193], v[42:45]
	s_waitcnt lgkmcnt(0)
	v_mfma_f32_16x16x32_bf16 v[66:69], v[210:213], v[164:167], v[66:69]
	v_mfma_f32_16x16x32_bf16 v[34:37], v[210:213], v[190:193], v[34:37]
	v_add_u32_e32 v216, v173, v175
	ds_read_b128 v[164:167], v216 offset:32768
	ds_read_b128 v[190:193], v216 offset:34816
	v_add_u32_e32 v217, v176, v175
	ds_read_b128 v[198:201], v217
	ds_read_b128 v[202:205], v217 offset:2048
	ds_read_b128 v[206:209], v217 offset:4096
	ds_read_b128 v[210:213], v217 offset:6144
	s_waitcnt lgkmcnt(3)
	v_mfma_f32_16x16x32_bf16 v[152:155], v[198:201], v[164:167], v[152:155]
	v_mfma_f32_16x16x32_bf16 v[62:65], v[198:201], v[190:193], v[62:65]
	s_waitcnt lgkmcnt(2)
	v_mfma_f32_16x16x32_bf16 v[120:123], v[202:205], v[164:167], v[120:123]
	v_mfma_f32_16x16x32_bf16 v[54:57], v[202:205], v[190:193], v[54:57]
	s_waitcnt lgkmcnt(1)
	v_mfma_f32_16x16x32_bf16 v[112:115], v[206:209], v[164:167], v[112:115]
	v_mfma_f32_16x16x32_bf16 v[46:49], v[206:209], v[190:193], v[46:49]
	s_waitcnt lgkmcnt(0)
	v_mfma_f32_16x16x32_bf16 v[70:73], v[210:213], v[164:167], v[70:73]
	v_mfma_f32_16x16x32_bf16 v[38:41], v[210:213], v[190:193], v[38:41]
	ds_read_b128 v[198:201], v217 offset:8192
	ds_read_b128 v[202:205], v217 offset:10240
	ds_read_b128 v[206:209], v217 offset:12288
	ds_read_b128 v[210:213], v217 offset:14336
	s_waitcnt lgkmcnt(3)
	v_mfma_f32_16x16x32_bf16 v[148:151], v[198:201], v[164:167], v[148:151]
	s_min_u32 s12, s0, 27
	s_waitcnt lgkmcnt(0)
	v_mfma_f32_16x16x32_bf16 v[116:119], v[202:205], v[164:167], v[116:119]
	s_barrier
	s_lshl_b32 s12, s12, 17
	v_mfma_f32_16x16x32_bf16 v[92:95], v[206:209], v[164:167], v[92:95]
	s_add_i32 s12, s12, 0x80000
	s_sub_i32 s58, s0, 28
	s_lshl_b32 s58, s58, 17
	s_add_i32 s58, s58, s85
	s_cmp_gt_u32 s0, 27
	s_cselect_b32 s12, s58, s12
	v_mfma_f32_16x16x32_bf16 v[66:69], v[210:213], v[164:167], v[66:69]
	s_min_u32 s43, s0, 29
	s_lshl_b32 s43, s43, 7
	s_waitcnt vmcnt(7)
	ds_write_b128 v189, v[132:135] offset:38912
	s_waitcnt vmcnt(6)
	ds_write_b128 v181, v[124:127] offset:39936
	s_waitcnt vmcnt(5)
	ds_write_b128 v189, v[140:143] offset:40960
	s_waitcnt vmcnt(4)
	ds_write_b128 v181, v[144:147] offset:41984
	s_addk_i32 s43, 0x100
	s_cmp_lt_u32 s0, 30
	s_cbranch_scc1 .Lxk_nx1
	s_cmp_eq_u32 s84, 0
	s_cbranch_scc1 .Lxk_nx1
	s_mov_b32 s43, 0
	v_lshl_or_b32 v182, v246, 12, v163
	v_lshl_or_b32 v183, v247, 12, v163
	v_lshl_or_b32 v184, v248, 12, v163
	v_lshl_or_b32 v185, v249, 12, v163
	v_lshl_or_b32 v186, v250, 12, v163
	v_lshl_or_b32 v187, v251, 12, v163
.Lxk_nx1:
	buffer_load_dwordx4 v[124:127], v182, s[4:7], s43 offen
	buffer_load_dwordx4 v[128:131], v183, s[4:7], s43 offen
	buffer_load_dwordx4 v[132:135], v184, s[4:7], s43 offen
	buffer_load_dwordx4 v[136:139], v185, s[4:7], s43 offen
	v_cvt_pk_bf16_f32 v164, v96, v100
	v_cvt_pk_bf16_f32 v165, v104, v108
	v_cvt_pk_bf16_f32 v96, v97, v101
	v_cvt_pk_bf16_f32 v97, v105, v109
	ds_write2_b64 v188, v[164:165], v[96:97] offset1:16
	v_cvt_pk_bf16_f32 v96, v98, v102
	v_cvt_pk_bf16_f32 v97, v106, v110
	v_cvt_pk_bf16_f32 v98, v99, v103
	v_cvt_pk_bf16_f32 v99, v107, v111
	ds_write2_b64 v180, v[96:97], v[98:99] offset0:32 offset1:48
	buffer_load_dwordx4 v[96:99], v160, s[8:11], s12 offen nt
	buffer_load_dwordx4 v[100:103], v90, s[8:11], s12 offen nt
	buffer_load_dwordx4 v[104:107], v178, s[8:11], s12 offen nt
	buffer_load_dwordx4 v[108:111], v179, s[8:11], s12 offen nt
	v_mfma_f32_16x16x32_bf16 v[58:61], v[198:201], v[190:193], v[58:61]
	v_mfma_f32_16x16x32_bf16 v[50:53], v[202:205], v[190:193], v[50:53]
	v_mfma_f32_16x16x32_bf16 v[42:45], v[206:209], v[190:193], v[42:45]
	v_mfma_f32_16x16x32_bf16 v[34:37], v[210:213], v[190:193], v[34:37]
	ds_read_b128 v[164:167], v214 offset:38912
	ds_read_b128 v[190:193], v214 offset:40960
	ds_read_b128 v[198:201], v215 offset:16384
	ds_read_b128 v[202:205], v215 offset:18432
	ds_read_b128 v[206:209], v215 offset:20480
	ds_read_b128 v[210:213], v215 offset:22528
	s_waitcnt lgkmcnt(3)
	v_mfma_f32_16x16x32_bf16 v[152:155], v[198:201], v[164:167], v[152:155]
	v_mfma_f32_16x16x32_bf16 v[62:65], v[198:201], v[190:193], v[62:65]
	s_waitcnt lgkmcnt(2)
	v_mfma_f32_16x16x32_bf16 v[120:123], v[202:205], v[164:167], v[120:123]
	v_mfma_f32_16x16x32_bf16 v[54:57], v[202:205], v[190:193], v[54:57]
	s_waitcnt lgkmcnt(1)
	v_mfma_f32_16x16x32_bf16 v[112:115], v[206:209], v[164:167], v[112:115]
	v_mfma_f32_16x16x32_bf16 v[46:49], v[206:209], v[190:193], v[46:49]
	s_waitcnt lgkmcnt(0)
	v_mfma_f32_16x16x32_bf16 v[70:73], v[210:213], v[164:167], v[70:73]
	v_mfma_f32_16x16x32_bf16 v[38:41], v[210:213], v[190:193], v[38:41]
	ds_read_b128 v[198:201], v215 offset:24576
	ds_read_b128 v[202:205], v215 offset:26624
	ds_read_b128 v[206:209], v215 offset:28672
	ds_read_b128 v[210:213], v215 offset:30720
	s_waitcnt lgkmcnt(3)
	v_mfma_f32_16x16x32_bf16 v[148:151], v[198:201], v[164:167], v[148:151]
	v_mfma_f32_16x16x32_bf16 v[58:61], v[198:201], v[190:193], v[58:61]
	s_waitcnt lgkmcnt(2)
	v_mfma_f32_16x16x32_bf16 v[116:119], v[202:205], v[164:167], v[116:119]
	v_mfma_f32_16x16x32_bf16 v[50:53], v[202:205], v[190:193], v[50:53]
	s_waitcnt lgkmcnt(1)
	v_mfma_f32_16x16x32_bf16 v[92:95], v[206:209], v[164:167], v[92:95]
	v_mfma_f32_16x16x32_bf16 v[42:45], v[206:209], v[190:193], v[42:45]
	s_waitcnt lgkmcnt(0)
	v_mfma_f32_16x16x32_bf16 v[66:69], v[210:213], v[164:167], v[66:69]
	v_mfma_f32_16x16x32_bf16 v[34:37], v[210:213], v[190:193], v[34:37]
	ds_read_b128 v[164:167], v216 offset:38912
	ds_read_b128 v[190:193], v216 offset:40960
	ds_read_b128 v[198:201], v217 offset:16384
	ds_read_b128 v[202:205], v217 offset:18432
	ds_read_b128 v[206:209], v217 offset:20480
	ds_read_b128 v[210:213], v217 offset:22528
	s_waitcnt lgkmcnt(3)
	v_mfma_f32_16x16x32_bf16 v[152:155], v[198:201], v[164:167], v[152:155]
	v_mfma_f32_16x16x32_bf16 v[62:65], v[198:201], v[190:193], v[62:65]
	s_waitcnt lgkmcnt(2)
	v_mfma_f32_16x16x32_bf16 v[120:123], v[202:205], v[164:167], v[120:123]
	v_mfma_f32_16x16x32_bf16 v[54:57], v[202:205], v[190:193], v[54:57]
	s_waitcnt lgkmcnt(1)
	v_mfma_f32_16x16x32_bf16 v[112:115], v[206:209], v[164:167], v[112:115]
	v_mfma_f32_16x16x32_bf16 v[46:49], v[206:209], v[190:193], v[46:49]
	s_waitcnt lgkmcnt(0)
	v_mfma_f32_16x16x32_bf16 v[70:73], v[210:213], v[164:167], v[70:73]
	v_mfma_f32_16x16x32_bf16 v[38:41], v[210:213], v[190:193], v[38:41]
	ds_read_b128 v[198:201], v217 offset:24576
	ds_read_b128 v[202:205], v217 offset:26624
	ds_read_b128 v[206:209], v217 offset:28672
	ds_read_b128 v[210:213], v217 offset:30720
	s_waitcnt lgkmcnt(3)
	v_mfma_f32_16x16x32_bf16 v[148:151], v[198:201], v[164:167], v[148:151]
	s_waitcnt lgkmcnt(0)
	s_barrier
	v_mfma_f32_16x16x32_bf16 v[58:61], v[198:201], v[190:193], v[58:61]
	v_mfma_f32_16x16x32_bf16 v[116:119], v[202:205], v[164:167], v[116:119]
	v_mfma_f32_16x16x32_bf16 v[50:53], v[202:205], v[190:193], v[50:53]
	v_mfma_f32_16x16x32_bf16 v[92:95], v[206:209], v[164:167], v[92:95]
	v_mfma_f32_16x16x32_bf16 v[42:45], v[206:209], v[190:193], v[42:45]
	v_mfma_f32_16x16x32_bf16 v[66:69], v[210:213], v[164:167], v[66:69]
	v_mfma_f32_16x16x32_bf16 v[34:37], v[210:213], v[190:193], v[34:37]
	s_lshl_b32 s1, s1, 7
	s_waitcnt vmcnt(7)
	ds_write_b128 v189, v[124:127] offset:32768
	s_waitcnt vmcnt(6)
	ds_write_b128 v181, v[128:131] offset:33792
	s_waitcnt vmcnt(5)
	ds_write_b128 v189, v[132:135] offset:34816
	s_waitcnt vmcnt(4)
	ds_write_b128 v181, v[136:139] offset:35840
	s_addk_i32 s1, 0x180
	s_cmp_eq_u32 s0, 30
	s_cselect_b32 s58, s84, 0
	s_cmp_lg_u32 s58, 0
	s_cselect_b32 s1, 0x80, s1
	buffer_load_dwordx4 v[132:135], v182, s[4:7], s1 offen
	buffer_load_dwordx4 v[124:127], v183, s[4:7], s1 offen
	buffer_load_dwordx4 v[140:143], v184, s[4:7], s1 offen
	buffer_load_dwordx4 v[144:147], v185, s[4:7], s1 offen
	s_cmp_gt_u32 s0, 29
	s_cbranch_scc0 .Lmoe_k_b

.LBB0_1785:
	s_add_i32 s2, s2, 2
	s_min_u32 s3, s2, 4
	s_lshl_b32 s33, s3, 19
	s_add_i32 s33, s33, 0x180000
	s_add_i32 s40, s85, 0x80000
	s_cmp_gt_u32 s2, 4
	s_cselect_b32 s33, s40, s33
	s_waitcnt vmcnt(10)
	v_cvt_pk_bf16_f32 v164, v2, v10
	s_waitcnt vmcnt(7)
	v_cvt_pk_bf16_f32 v165, v6, v14
	v_cvt_pk_bf16_f32 v166, v3, v11
	v_cvt_pk_bf16_f32 v167, v7, v15
	v_cvt_pk_bf16_f32 v190, v4, v12
	v_cvt_pk_bf16_f32 v191, v8, v16
	v_cvt_pk_bf16_f32 v192, v5, v13
	v_cvt_pk_bf16_f32 v193, v9, v17
	buffer_load_dwordx4 v[2:5], v160, s[8:11], s33 offen nt
	buffer_load_dwordx4 v[10:13], v90, s[8:11], s33 offen nt
	buffer_load_dwordx4 v[6:9], v178, s[8:11], s33 offen nt
	buffer_load_dwordx4 v[14:17], v179, s[8:11], s33 offen nt
	v_add_u32_e32 v194, 0x4000, v188
	v_add_u32_e32 v195, 0x4000, v180
	v_add_u32_e32 v214, v173, v174
	ds_write2_b64 v194, v[164:165], v[166:167] offset1:16
	ds_write2_b64 v195, v[190:191], v[192:193] offset0:32 offset1:48
	v_add_u32_e32 v215, v176, v174
	ds_read_b128 v[164:167], v214 offset:32768
	ds_read_b128 v[190:193], v214 offset:34816
	ds_read_b128 v[194:197], v214 offset:36864
	ds_read_b128 v[198:201], v215
	ds_read_b128 v[202:205], v215 offset:2048
	ds_read_b128 v[206:209], v215 offset:4096
	ds_read_b128 v[210:213], v215 offset:6144
	s_waitcnt lgkmcnt(3)
	v_mfma_f32_16x16x32_bf16 v[152:155], v[198:201], v[164:167], v[152:155]
	v_mfma_f32_16x16x32_bf16 v[120:123], v[198:201], v[190:193], v[120:123]
	v_mfma_f32_16x16x32_bf16 v[62:65], v[198:201], v[194:197], v[62:65]
	s_waitcnt lgkmcnt(2)
	v_mfma_f32_16x16x32_bf16 v[148:151], v[202:205], v[164:167], v[148:151]
	v_mfma_f32_16x16x32_bf16 v[96:99], v[202:205], v[190:193], v[96:99]
	v_mfma_f32_16x16x32_bf16 v[58:61], v[202:205], v[194:197], v[58:61]
	s_waitcnt lgkmcnt(1)
	v_mfma_f32_16x16x32_bf16 v[144:147], v[206:209], v[164:167], v[144:147]
	v_mfma_f32_16x16x32_bf16 v[86:89], v[206:209], v[190:193], v[86:89]
	v_mfma_f32_16x16x32_bf16 v[54:57], v[206:209], v[194:197], v[54:57]
	s_waitcnt lgkmcnt(0)
	v_mfma_f32_16x16x32_bf16 v[140:143], v[210:213], v[164:167], v[140:143]
	v_mfma_f32_16x16x32_bf16 v[82:85], v[210:213], v[190:193], v[82:85]
	v_mfma_f32_16x16x32_bf16 v[50:53], v[210:213], v[194:197], v[50:53]
	ds_read_b128 v[198:201], v215 offset:8192
	ds_read_b128 v[202:205], v215 offset:10240
	ds_read_b128 v[206:209], v215 offset:12288
	ds_read_b128 v[210:213], v215 offset:14336
	s_waitcnt lgkmcnt(3)
	v_mfma_f32_16x16x32_bf16 v[136:139], v[198:201], v[164:167], v[136:139]
	v_mfma_f32_16x16x32_bf16 v[78:81], v[198:201], v[190:193], v[78:81]
	v_mfma_f32_16x16x32_bf16 v[46:49], v[198:201], v[194:197], v[46:49]
	s_waitcnt lgkmcnt(2)
	v_mfma_f32_16x16x32_bf16 v[132:135], v[202:205], v[164:167], v[132:135]
	v_mfma_f32_16x16x32_bf16 v[74:77], v[202:205], v[190:193], v[74:77]
	v_mfma_f32_16x16x32_bf16 v[42:45], v[202:205], v[194:197], v[42:45]
	s_waitcnt lgkmcnt(1)
	v_mfma_f32_16x16x32_bf16 v[128:131], v[206:209], v[164:167], v[128:131]
	v_mfma_f32_16x16x32_bf16 v[70:73], v[206:209], v[190:193], v[70:73]
	v_mfma_f32_16x16x32_bf16 v[38:41], v[206:209], v[194:197], v[38:41]
	s_waitcnt lgkmcnt(0)
	v_mfma_f32_16x16x32_bf16 v[124:127], v[210:213], v[164:167], v[124:127]
	v_mfma_f32_16x16x32_bf16 v[66:69], v[210:213], v[190:193], v[66:69]
	v_mfma_f32_16x16x32_bf16 v[34:37], v[210:213], v[194:197], v[34:37]
	v_add_u32_e32 v216, v173, v175
	ds_read_b128 v[164:167], v216 offset:32768
	ds_read_b128 v[190:193], v216 offset:34816
	v_add_u32_e32 v217, v176, v175
	ds_read_b128 v[194:197], v216 offset:36864
	ds_read_b128 v[198:201], v217
	ds_read_b128 v[202:205], v217 offset:2048
	ds_read_b128 v[206:209], v217 offset:4096
	ds_read_b128 v[210:213], v217 offset:6144
	s_waitcnt lgkmcnt(3)
	v_mfma_f32_16x16x32_bf16 v[152:155], v[198:201], v[164:167], v[152:155]
	v_mfma_f32_16x16x32_bf16 v[120:123], v[198:201], v[190:193], v[120:123]
	v_mfma_f32_16x16x32_bf16 v[62:65], v[198:201], v[194:197], v[62:65]
	s_waitcnt lgkmcnt(2)
	v_mfma_f32_16x16x32_bf16 v[148:151], v[202:205], v[164:167], v[148:151]
	v_mfma_f32_16x16x32_bf16 v[96:99], v[202:205], v[190:193], v[96:99]
	v_mfma_f32_16x16x32_bf16 v[58:61], v[202:205], v[194:197], v[58:61]
	s_waitcnt lgkmcnt(1)
	v_mfma_f32_16x16x32_bf16 v[144:147], v[206:209], v[164:167], v[144:147]
	v_mfma_f32_16x16x32_bf16 v[86:89], v[206:209], v[190:193], v[86:89]
	v_mfma_f32_16x16x32_bf16 v[54:57], v[206:209], v[194:197], v[54:57]
	s_waitcnt lgkmcnt(0)
	v_mfma_f32_16x16x32_bf16 v[140:143], v[210:213], v[164:167], v[140:143]
	v_mfma_f32_16x16x32_bf16 v[82:85], v[210:213], v[190:193], v[82:85]
	v_mfma_f32_16x16x32_bf16 v[50:53], v[210:213], v[194:197], v[50:53]
	ds_read_b128 v[198:201], v217 offset:8192
	ds_read_b128 v[202:205], v217 offset:10240
	ds_read_b128 v[206:209], v217 offset:12288
	ds_read_b128 v[210:213], v217 offset:14336
	s_waitcnt lgkmcnt(3)
	v_mfma_f32_16x16x32_bf16 v[136:139], v[198:201], v[164:167], v[136:139]
	s_min_u32 s33, s2, 3
	s_waitcnt lgkmcnt(0)
	v_mfma_f32_16x16x32_bf16 v[132:135], v[202:205], v[164:167], v[132:135]
	s_barrier
	s_lshl_b32 s33, s33, 19
	v_mfma_f32_16x16x32_bf16 v[128:131], v[206:209], v[164:167], v[128:131]
	s_bitset1_b32 s33, 21
	s_sub_i32 s40, s2, 4
	s_lshl_b32 s40, s40, 19
	s_add_i32 s40, s40, s85
	s_cmp_gt_u32 s2, 3
	s_cselect_b32 s33, s40, s33
	v_mfma_f32_16x16x32_bf16 v[124:127], v[210:213], v[164:167], v[124:127]
	s_min_u32 s43, s2, 5
	s_lshl_b32 s43, s43, 7
	s_waitcnt vmcnt(9)
	ds_write_b128 v189, v[104:107] offset:38912
	s_waitcnt vmcnt(8)
	ds_write_b128 v181, v[92:95] offset:39936
	s_waitcnt vmcnt(7)
	ds_write_b128 v189, v[112:115] offset:40960
	s_waitcnt vmcnt(6)
	ds_write_b128 v181, v[116:119] offset:41984
	s_waitcnt vmcnt(5)
	ds_write_b128 v189, v[100:103] offset:43008
	s_waitcnt vmcnt(4)
	ds_write_b128 v181, v[108:111] offset:44032
	s_addk_i32 s43, 0x100
	s_cmp_lt_u32 s2, 6
	s_cbranch_scc1 .Lxl_nx0
	s_cmp_eq_u32 s84, 0
	s_cbranch_scc1 .Lxl_nx0
	s_mov_b32 s43, 0
	v_add_u32_e32 v252, s87, v162
	v_min_i32_e32 v253, s86, v252
	v_add_u32_e32 v253, s88, v253
	v_lshl_or_b32 v182, v253, 10, v163
	v_or_b32_e32 v253, 8, v252
	v_min_i32_e32 v253, s86, v253
	v_add_u32_e32 v253, s88, v253
	v_lshl_or_b32 v183, v253, 10, v163
	v_add_u32_e32 v253, 0x80, v252
	v_min_i32_e32 v253, s86, v253
	v_add_u32_e32 v253, s88, v253
	v_lshl_or_b32 v184, v253, 10, v163
	v_add_u32_e32 v253, 0x88, v252
	v_min_i32_e32 v253, s86, v253
	v_add_u32_e32 v253, s88, v253
	v_lshl_or_b32 v185, v253, 10, v163
	v_add_u32_e32 v253, 0x100, v252
	v_min_i32_e32 v253, s86, v253
	v_add_u32_e32 v253, s88, v253
	v_lshl_or_b32 v186, v253, 10, v163
	v_add_u32_e32 v253, 0x108, v252
	v_min_i32_e32 v253, s86, v253
	v_add_u32_e32 v253, s88, v253
	v_lshl_or_b32 v187, v253, 10, v163
.Lxl_nx0:
	buffer_load_dwordx4 v[92:95], v182, s[4:7], s43 offen
	buffer_load_dwordx4 v[100:103], v183, s[4:7], s43 offen
	buffer_load_dwordx4 v[104:107], v184, s[4:7], s43 offen
	buffer_load_dwordx4 v[108:111], v185, s[4:7], s43 offen
	buffer_load_dwordx4 v[112:115], v186, s[4:7], s43 offen
	buffer_load_dwordx4 v[116:119], v187, s[4:7], s43 offen
	v_cvt_pk_bf16_f32 v164, v18, v22
	v_cvt_pk_bf16_f32 v165, v26, v30
	v_cvt_pk_bf16_f32 v18, v19, v23
	v_cvt_pk_bf16_f32 v19, v27, v31
	ds_write2_b64 v188, v[164:165], v[18:19] offset1:16
	v_cvt_pk_bf16_f32 v18, v20, v24
	v_cvt_pk_bf16_f32 v19, v28, v32
	v_cvt_pk_bf16_f32 v20, v21, v25
	v_cvt_pk_bf16_f32 v21, v29, v33
	ds_write2_b64 v180, v[18:19], v[20:21] offset0:32 offset1:48
	buffer_load_dwordx4 v[18:21], v160, s[8:11], s33 offen nt
	buffer_load_dwordx4 v[22:25], v90, s[8:11], s33 offen nt
	buffer_load_dwordx4 v[26:29], v178, s[8:11], s33 offen nt
	buffer_load_dwordx4 v[30:33], v179, s[8:11], s33 offen nt
	v_mfma_f32_16x16x32_bf16 v[78:81], v[198:201], v[190:193], v[78:81]
	v_mfma_f32_16x16x32_bf16 v[46:49], v[198:201], v[194:197], v[46:49]
	v_mfma_f32_16x16x32_bf16 v[74:77], v[202:205], v[190:193], v[74:77]
	v_mfma_f32_16x16x32_bf16 v[42:45], v[202:205], v[194:197], v[42:45]
	v_mfma_f32_16x16x32_bf16 v[70:73], v[206:209], v[190:193], v[70:73]
	v_mfma_f32_16x16x32_bf16 v[38:41], v[206:209], v[194:197], v[38:41]
	v_mfma_f32_16x16x32_bf16 v[66:69], v[210:213], v[190:193], v[66:69]
	v_mfma_f32_16x16x32_bf16 v[34:37], v[210:213], v[194:197], v[34:37]
	ds_read_b128 v[164:167], v214 offset:38912
	ds_read_b128 v[190:193], v214 offset:40960
	ds_read_b128 v[194:197], v214 offset:43008
	ds_read_b128 v[198:201], v215 offset:16384
	ds_read_b128 v[202:205], v215 offset:18432
	ds_read_b128 v[206:209], v215 offset:20480
	ds_read_b128 v[210:213], v215 offset:22528
	s_waitcnt lgkmcnt(3)
	v_mfma_f32_16x16x32_bf16 v[152:155], v[198:201], v[164:167], v[152:155]
	v_mfma_f32_16x16x32_bf16 v[120:123], v[198:201], v[190:193], v[120:123]
	v_mfma_f32_16x16x32_bf16 v[62:65], v[198:201], v[194:197], v[62:65]
	s_waitcnt lgkmcnt(2)
	v_mfma_f32_16x16x32_bf16 v[148:151], v[202:205], v[164:167], v[148:151]
	v_mfma_f32_16x16x32_bf16 v[96:99], v[202:205], v[190:193], v[96:99]
	v_mfma_f32_16x16x32_bf16 v[58:61], v[202:205], v[194:197], v[58:61]
	s_waitcnt lgkmcnt(1)
	v_mfma_f32_16x16x32_bf16 v[144:147], v[206:209], v[164:167], v[144:147]
	v_mfma_f32_16x16x32_bf16 v[86:89], v[206:209], v[190:193], v[86:89]
	v_mfma_f32_16x16x32_bf16 v[54:57], v[206:209], v[194:197], v[54:57]
	s_waitcnt lgkmcnt(0)
	v_mfma_f32_16x16x32_bf16 v[140:143], v[210:213], v[164:167], v[140:143]
	v_mfma_f32_16x16x32_bf16 v[82:85], v[210:213], v[190:193], v[82:85]
	v_mfma_f32_16x16x32_bf16 v[50:53], v[210:213], v[194:197], v[50:53]
	ds_read_b128 v[198:201], v215 offset:24576
	ds_read_b128 v[202:205], v215 offset:26624
	ds_read_b128 v[206:209], v215 offset:28672
	ds_read_b128 v[210:213], v215 offset:30720
	s_waitcnt lgkmcnt(3)
	v_mfma_f32_16x16x32_bf16 v[136:139], v[198:201], v[164:167], v[136:139]
	v_mfma_f32_16x16x32_bf16 v[78:81], v[198:201], v[190:193], v[78:81]
	v_mfma_f32_16x16x32_bf16 v[46:49], v[198:201], v[194:197], v[46:49]
	s_waitcnt lgkmcnt(2)
	v_mfma_f32_16x16x32_bf16 v[132:135], v[202:205], v[164:167], v[132:135]
	v_mfma_f32_16x16x32_bf16 v[74:77], v[202:205], v[190:193], v[74:77]
	v_mfma_f32_16x16x32_bf16 v[42:45], v[202:205], v[194:197], v[42:45]
	s_waitcnt lgkmcnt(1)
	v_mfma_f32_16x16x32_bf16 v[128:131], v[206:209], v[164:167], v[128:131]
	v_mfma_f32_16x16x32_bf16 v[70:73], v[206:209], v[190:193], v[70:73]
	v_mfma_f32_16x16x32_bf16 v[38:41], v[206:209], v[194:197], v[38:41]
	s_waitcnt lgkmcnt(0)
	v_mfma_f32_16x16x32_bf16 v[124:127], v[210:213], v[164:167], v[124:127]
	v_mfma_f32_16x16x32_bf16 v[66:69], v[210:213], v[190:193], v[66:69]
	v_mfma_f32_16x16x32_bf16 v[34:37], v[210:213], v[194:197], v[34:37]
	ds_read_b128 v[164:167], v216 offset:38912
	ds_read_b128 v[190:193], v216 offset:40960
	ds_read_b128 v[194:197], v216 offset:43008
	ds_read_b128 v[198:201], v217 offset:16384
	ds_read_b128 v[202:205], v217 offset:18432
	ds_read_b128 v[206:209], v217 offset:20480
	ds_read_b128 v[210:213], v217 offset:22528
	s_waitcnt lgkmcnt(3)
	v_mfma_f32_16x16x32_bf16 v[152:155], v[198:201], v[164:167], v[152:155]
	v_mfma_f32_16x16x32_bf16 v[120:123], v[198:201], v[190:193], v[120:123]
	v_mfma_f32_16x16x32_bf16 v[62:65], v[198:201], v[194:197], v[62:65]
	s_waitcnt lgkmcnt(2)
	v_mfma_f32_16x16x32_bf16 v[148:151], v[202:205], v[164:167], v[148:151]
	v_mfma_f32_16x16x32_bf16 v[96:99], v[202:205], v[190:193], v[96:99]
	v_mfma_f32_16x16x32_bf16 v[58:61], v[202:205], v[194:197], v[58:61]
	s_waitcnt lgkmcnt(1)
	v_mfma_f32_16x16x32_bf16 v[144:147], v[206:209], v[164:167], v[144:147]
	v_mfma_f32_16x16x32_bf16 v[86:89], v[206:209], v[190:193], v[86:89]
	v_mfma_f32_16x16x32_bf16 v[54:57], v[206:209], v[194:197], v[54:57]
	s_waitcnt lgkmcnt(0)
	v_mfma_f32_16x16x32_bf16 v[140:143], v[210:213], v[164:167], v[140:143]
	v_mfma_f32_16x16x32_bf16 v[82:85], v[210:213], v[190:193], v[82:85]
	v_mfma_f32_16x16x32_bf16 v[50:53], v[210:213], v[194:197], v[50:53]
	ds_read_b128 v[198:201], v217 offset:24576
	ds_read_b128 v[202:205], v217 offset:26624
	ds_read_b128 v[206:209], v217 offset:28672
	ds_read_b128 v[210:213], v217 offset:30720
	s_waitcnt lgkmcnt(3)
	v_mfma_f32_16x16x32_bf16 v[136:139], v[198:201], v[164:167], v[136:139]
	s_waitcnt lgkmcnt(0)
	s_barrier
	v_mfma_f32_16x16x32_bf16 v[78:81], v[198:201], v[190:193], v[78:81]
	v_mfma_f32_16x16x32_bf16 v[46:49], v[198:201], v[194:197], v[46:49]
	v_mfma_f32_16x16x32_bf16 v[132:135], v[202:205], v[164:167], v[132:135]
	v_mfma_f32_16x16x32_bf16 v[74:77], v[202:205], v[190:193], v[74:77]
	v_mfma_f32_16x16x32_bf16 v[42:45], v[202:205], v[194:197], v[42:45]
	v_mfma_f32_16x16x32_bf16 v[128:131], v[206:209], v[164:167], v[128:131]
	v_mfma_f32_16x16x32_bf16 v[70:73], v[206:209], v[190:193], v[70:73]
	v_mfma_f32_16x16x32_bf16 v[38:41], v[206:209], v[194:197], v[38:41]
	v_mfma_f32_16x16x32_bf16 v[124:127], v[210:213], v[164:167], v[124:127]
	v_mfma_f32_16x16x32_bf16 v[66:69], v[210:213], v[190:193], v[66:69]
	v_mfma_f32_16x16x32_bf16 v[34:37], v[210:213], v[194:197], v[34:37]
	s_lshl_b32 s3, s3, 7
	s_waitcnt vmcnt(9)
	ds_write_b128 v189, v[92:95] offset:32768
	s_waitcnt vmcnt(8)
	ds_write_b128 v181, v[100:103] offset:33792
	s_waitcnt vmcnt(7)
	ds_write_b128 v189, v[104:107] offset:34816
	s_waitcnt vmcnt(6)
	ds_write_b128 v181, v[108:111] offset:35840
	s_waitcnt vmcnt(5)
	ds_write_b128 v189, v[112:115] offset:36864
	s_waitcnt vmcnt(4)
	ds_write_b128 v181, v[116:119] offset:37888
	s_addk_i32 s3, 0x180
	s_cmp_eq_u32 s2, 6
	s_cselect_b32 s40, s84, 0
	s_cmp_lg_u32 s40, 0
	s_cselect_b32 s3, 0x80, s3
	buffer_load_dwordx4 v[104:107], v182, s[4:7], s3 offen
	buffer_load_dwordx4 v[92:95], v183, s[4:7], s3 offen
	buffer_load_dwordx4 v[112:115], v184, s[4:7], s3 offen
	buffer_load_dwordx4 v[116:119], v185, s[4:7], s3 offen
	buffer_load_dwordx4 v[100:103], v186, s[4:7], s3 offen
	buffer_load_dwordx4 v[108:111], v187, s[4:7], s3 offen
	s_cmp_gt_u32 s2, 5
	s_cbranch_scc0 .LBB0_1785
	s_branch .Lmoe_l_done
.Lmoe_l_b:
	s_add_i32 s2, s2, 2
	s_min_u32 s3, s2, 4
	s_lshl_b32 s33, s3, 19
	s_add_i32 s33, s33, 0x180000
	s_add_i32 s40, s85, 0x80000
	s_cmp_gt_u32 s2, 4
	s_cselect_b32 s33, s40, s33
	s_waitcnt vmcnt(10)
	v_cvt_pk_bf16_f32 v164, v2, v10
	s_waitcnt vmcnt(7)
	v_cvt_pk_bf16_f32 v165, v6, v14
	v_cvt_pk_bf16_f32 v166, v3, v11
	v_cvt_pk_bf16_f32 v167, v7, v15
	v_cvt_pk_bf16_f32 v190, v4, v12
	v_cvt_pk_bf16_f32 v191, v8, v16
	v_cvt_pk_bf16_f32 v192, v5, v13
	v_cvt_pk_bf16_f32 v193, v9, v17
	buffer_load_dwordx4 v[2:5], v160, s[8:11], s33 offen nt
	buffer_load_dwordx4 v[10:13], v90, s[8:11], s33 offen nt
	buffer_load_dwordx4 v[6:9], v178, s[8:11], s33 offen nt
	buffer_load_dwordx4 v[14:17], v179, s[8:11], s33 offen nt
	v_add_u32_e32 v194, 0x4000, v188
	v_add_u32_e32 v195, 0x4000, v180
	v_add_u32_e32 v214, v173, v174
	ds_write2_b64 v194, v[164:165], v[166:167] offset1:16
	ds_write2_b64 v195, v[190:191], v[192:193] offset0:32 offset1:48
	v_add_u32_e32 v215, v176, v174
	ds_read_b128 v[164:167], v214 offset:32768
	ds_read_b128 v[190:193], v214 offset:34816
	ds_read_b128 v[198:201], v215
	ds_read_b128 v[202:205], v215 offset:2048
	ds_read_b128 v[206:209], v215 offset:4096
	ds_read_b128 v[210:213], v215 offset:6144
	s_waitcnt lgkmcnt(3)
	v_mfma_f32_16x16x32_bf16 v[152:155], v[198:201], v[164:167], v[152:155]
	v_mfma_f32_16x16x32_bf16 v[120:123], v[198:201], v[190:193], v[120:123]
	s_waitcnt lgkmcnt(2)
	v_mfma_f32_16x16x32_bf16 v[148:151], v[202:205], v[164:167], v[148:151]
	v_mfma_f32_16x16x32_bf16 v[96:99], v[202:205], v[190:193], v[96:99]
	s_waitcnt lgkmcnt(1)
	v_mfma_f32_16x16x32_bf16 v[144:147], v[206:209], v[164:167], v[144:147]
	v_mfma_f32_16x16x32_bf16 v[86:89], v[206:209], v[190:193], v[86:89]
	s_waitcnt lgkmcnt(0)
	v_mfma_f32_16x16x32_bf16 v[140:143], v[210:213], v[164:167], v[140:143]
	v_mfma_f32_16x16x32_bf16 v[82:85], v[210:213], v[190:193], v[82:85]
	ds_read_b128 v[198:201], v215 offset:8192
	ds_read_b128 v[202:205], v215 offset:10240
	ds_read_b128 v[206:209], v215 offset:12288
	ds_read_b128 v[210:213], v215 offset:14336
	s_waitcnt lgkmcnt(3)
	v_mfma_f32_16x16x32_bf16 v[136:139], v[198:201], v[164:167], v[136:139]
	v_mfma_f32_16x16x32_bf16 v[78:81], v[198:201], v[190:193], v[78:81]
	s_waitcnt lgkmcnt(2)
	v_mfma_f32_16x16x32_bf16 v[132:135], v[202:205], v[164:167], v[132:135]
	v_mfma_f32_16x16x32_bf16 v[74:77], v[202:205], v[190:193], v[74:77]
	s_waitcnt lgkmcnt(1)
	v_mfma_f32_16x16x32_bf16 v[128:131], v[206:209], v[164:167], v[128:131]
	v_mfma_f32_16x16x32_bf16 v[70:73], v[206:209], v[190:193], v[70:73]
	s_waitcnt lgkmcnt(0)
	v_mfma_f32_16x16x32_bf16 v[124:127], v[210:213], v[164:167], v[124:127]
	v_mfma_f32_16x16x32_bf16 v[66:69], v[210:213], v[190:193], v[66:69]
	v_add_u32_e32 v216, v173, v175
	ds_read_b128 v[164:167], v216 offset:32768
	ds_read_b128 v[190:193], v216 offset:34816
	v_add_u32_e32 v217, v176, v175
	ds_read_b128 v[198:201], v217
	ds_read_b128 v[202:205], v217 offset:2048
	ds_read_b128 v[206:209], v217 offset:4096
	ds_read_b128 v[210:213], v217 offset:6144
	s_waitcnt lgkmcnt(3)
	v_mfma_f32_16x16x32_bf16 v[152:155], v[198:201], v[164:167], v[152:155]
	v_mfma_f32_16x16x32_bf16 v[120:123], v[198:201], v[190:193], v[120:123]
	s_waitcnt lgkmcnt(2)
	v_mfma_f32_16x16x32_bf16 v[148:151], v[202:205], v[164:167], v[148:151]
	v_mfma_f32_16x16x32_bf16 v[96:99], v[202:205], v[190:193], v[96:99]
	s_waitcnt lgkmcnt(1)
	v_mfma_f32_16x16x32_bf16 v[144:147], v[206:209], v[164:167], v[144:147]
	v_mfma_f32_16x16x32_bf16 v[86:89], v[206:209], v[190:193], v[86:89]
	s_waitcnt lgkmcnt(0)
	v_mfma_f32_16x16x32_bf16 v[140:143], v[210:213], v[164:167], v[140:143]
	v_mfma_f32_16x16x32_bf16 v[82:85], v[210:213], v[190:193], v[82:85]
	ds_read_b128 v[198:201], v217 offset:8192
	ds_read_b128 v[202:205], v217 offset:10240
	ds_read_b128 v[206:209], v217 offset:12288
	ds_read_b128 v[210:213], v217 offset:14336
	s_waitcnt lgkmcnt(3)
	v_mfma_f32_16x16x32_bf16 v[136:139], v[198:201], v[164:167], v[136:139]
	s_min_u32 s33, s2, 3
	s_waitcnt lgkmcnt(0)
	v_mfma_f32_16x16x32_bf16 v[132:135], v[202:205], v[164:167], v[132:135]
	s_barrier
	s_lshl_b32 s33, s33, 19
	v_mfma_f32_16x16x32_bf16 v[128:131], v[206:209], v[164:167], v[128:131]
	s_bitset1_b32 s33, 21
	s_sub_i32 s40, s2, 4
	s_lshl_b32 s40, s40, 19
	s_add_i32 s40, s40, s85
	s_cmp_gt_u32 s2, 3
	s_cselect_b32 s33, s40, s33
	v_mfma_f32_16x16x32_bf16 v[124:127], v[210:213], v[164:167], v[124:127]
	s_min_u32 s43, s2, 5
	s_lshl_b32 s43, s43, 7
	s_waitcnt vmcnt(7)
	ds_write_b128 v189, v[104:107] offset:38912
	s_waitcnt vmcnt(6)
	ds_write_b128 v181, v[92:95] offset:39936
	s_waitcnt vmcnt(5)
	ds_write_b128 v189, v[112:115] offset:40960
	s_waitcnt vmcnt(4)
	ds_write_b128 v181, v[116:119] offset:41984
	s_addk_i32 s43, 0x100
	s_cmp_lt_u32 s2, 6
	s_cbranch_scc1 .Lxl_nx1
	s_cmp_eq_u32 s84, 0
	s_cbranch_scc1 .Lxl_nx1
	s_mov_b32 s43, 0
	v_add_u32_e32 v252, s87, v162
	v_min_i32_e32 v253, s86, v252
	v_add_u32_e32 v253, s88, v253
	v_lshl_or_b32 v182, v253, 10, v163
	v_or_b32_e32 v253, 8, v252
	v_min_i32_e32 v253, s86, v253
	v_add_u32_e32 v253, s88, v253
	v_lshl_or_b32 v183, v253, 10, v163
	v_add_u32_e32 v253, 0x80, v252
	v_min_i32_e32 v253, s86, v253
	v_add_u32_e32 v253, s88, v253
	v_lshl_or_b32 v184, v253, 10, v163
	v_add_u32_e32 v253, 0x88, v252
	v_min_i32_e32 v253, s86, v253
	v_add_u32_e32 v253, s88, v253
	v_lshl_or_b32 v185, v253, 10, v163
	v_add_u32_e32 v253, 0x100, v252
	v_min_i32_e32 v253, s86, v253
	v_add_u32_e32 v253, s88, v253
	v_lshl_or_b32 v186, v253, 10, v163
	v_add_u32_e32 v253, 0x108, v252
	v_min_i32_e32 v253, s86, v253
	v_add_u32_e32 v253, s88, v253
	v_lshl_or_b32 v187, v253, 10, v163
.Lxl_nx1:
	buffer_load_dwordx4 v[92:95], v182, s[4:7], s43 offen
	buffer_load_dwordx4 v[100:103], v183, s[4:7], s43 offen
	buffer_load_dwordx4 v[104:107], v184, s[4:7], s43 offen
	buffer_load_dwordx4 v[108:111], v185, s[4:7], s43 offen
	v_cvt_pk_bf16_f32 v164, v18, v22
	v_cvt_pk_bf16_f32 v165, v26, v30
	v_cvt_pk_bf16_f32 v18, v19, v23
	v_cvt_pk_bf16_f32 v19, v27, v31
	ds_write2_b64 v188, v[164:165], v[18:19] offset1:16
	v_cvt_pk_bf16_f32 v18, v20, v24
	v_cvt_pk_bf16_f32 v19, v28, v32
	v_cvt_pk_bf16_f32 v20, v21, v25
	v_cvt_pk_bf16_f32 v21, v29, v33
	ds_write2_b64 v180, v[18:19], v[20:21] offset0:32 offset1:48
	buffer_load_dwordx4 v[18:21], v160, s[8:11], s33 offen nt
	buffer_load_dwordx4 v[22:25], v90, s[8:11], s33 offen nt
	buffer_load_dwordx4 v[26:29], v178, s[8:11], s33 offen nt
	buffer_load_dwordx4 v[30:33], v179, s[8:11], s33 offen nt
	v_mfma_f32_16x16x32_bf16 v[78:81], v[198:201], v[190:193], v[78:81]
	v_mfma_f32_16x16x32_bf16 v[74:77], v[202:205], v[190:193], v[74:77]
	v_mfma_f32_16x16x32_bf16 v[70:73], v[206:209], v[190:193], v[70:73]
	v_mfma_f32_16x16x32_bf16 v[66:69], v[210:213], v[190:193], v[66:69]
	ds_read_b128 v[164:167], v214 offset:38912
	ds_read_b128 v[190:193], v214 offset:40960
	ds_read_b128 v[198:201], v215 offset:16384
	ds_read_b128 v[202:205], v215 offset:18432
	ds_read_b128 v[206:209], v215 offset:20480
	ds_read_b128 v[210:213], v215 offset:22528
	s_waitcnt lgkmcnt(3)
	v_mfma_f32_16x16x32_bf16 v[152:155], v[198:201], v[164:167], v[152:155]
	v_mfma_f32_16x16x32_bf16 v[120:123], v[198:201], v[190:193], v[120:123]
	s_waitcnt lgkmcnt(2)
	v_mfma_f32_16x16x32_bf16 v[148:151], v[202:205], v[164:167], v[148:151]
	v_mfma_f32_16x16x32_bf16 v[96:99], v[202:205], v[190:193], v[96:99]
	s_waitcnt lgkmcnt(1)
	v_mfma_f32_16x16x32_bf16 v[144:147], v[206:209], v[164:167], v[144:147]
	v_mfma_f32_16x16x32_bf16 v[86:89], v[206:209], v[190:193], v[86:89]
	s_waitcnt lgkmcnt(0)
	v_mfma_f32_16x16x32_bf16 v[140:143], v[210:213], v[164:167], v[140:143]
	v_mfma_f32_16x16x32_bf16 v[82:85], v[210:213], v[190:193], v[82:85]
	ds_read_b128 v[198:201], v215 offset:24576
	ds_read_b128 v[202:205], v215 offset:26624
	ds_read_b128 v[206:209], v215 offset:28672
	ds_read_b128 v[210:213], v215 offset:30720
	s_waitcnt lgkmcnt(3)
	v_mfma_f32_16x16x32_bf16 v[136:139], v[198:201], v[164:167], v[136:139]
	v_mfma_f32_16x16x32_bf16 v[78:81], v[198:201], v[190:193], v[78:81]
	s_waitcnt lgkmcnt(2)
	v_mfma_f32_16x16x32_bf16 v[132:135], v[202:205], v[164:167], v[132:135]
	v_mfma_f32_16x16x32_bf16 v[74:77], v[202:205], v[190:193], v[74:77]
	s_waitcnt lgkmcnt(1)
	v_mfma_f32_16x16x32_bf16 v[128:131], v[206:209], v[164:167], v[128:131]
	v_mfma_f32_16x16x32_bf16 v[70:73], v[206:209], v[190:193], v[70:73]
	s_waitcnt lgkmcnt(0)
	v_mfma_f32_16x16x32_bf16 v[124:127], v[210:213], v[164:167], v[124:127]
	v_mfma_f32_16x16x32_bf16 v[66:69], v[210:213], v[190:193], v[66:69]
	ds_read_b128 v[164:167], v216 offset:38912
	ds_read_b128 v[190:193], v216 offset:40960
	ds_read_b128 v[198:201], v217 offset:16384
	ds_read_b128 v[202:205], v217 offset:18432
	ds_read_b128 v[206:209], v217 offset:20480
	ds_read_b128 v[210:213], v217 offset:22528
	s_waitcnt lgkmcnt(3)
	v_mfma_f32_16x16x32_bf16 v[152:155], v[198:201], v[164:167], v[152:155]
	v_mfma_f32_16x16x32_bf16 v[120:123], v[198:201], v[190:193], v[120:123]
	s_waitcnt lgkmcnt(2)
	v_mfma_f32_16x16x32_bf16 v[148:151], v[202:205], v[164:167], v[148:151]
	v_mfma_f32_16x16x32_bf16 v[96:99], v[202:205], v[190:193], v[96:99]
	s_waitcnt lgkmcnt(1)
	v_mfma_f32_16x16x32_bf16 v[144:147], v[206:209], v[164:167], v[144:147]
	v_mfma_f32_16x16x32_bf16 v[86:89], v[206:209], v[190:193], v[86:89]
	s_waitcnt lgkmcnt(0)
	v_mfma_f32_16x16x32_bf16 v[140:143], v[210:213], v[164:167], v[140:143]
	v_mfma_f32_16x16x32_bf16 v[82:85], v[210:213], v[190:193], v[82:85]
	ds_read_b128 v[198:201], v217 offset:24576
	ds_read_b128 v[202:205], v217 offset:26624
	ds_read_b128 v[206:209], v217 offset:28672
	ds_read_b128 v[210:213], v217 offset:30720
	s_waitcnt lgkmcnt(3)
	v_mfma_f32_16x16x32_bf16 v[136:139], v[198:201], v[164:167], v[136:139]
	s_waitcnt lgkmcnt(0)
	s_barrier
	v_mfma_f32_16x16x32_bf16 v[78:81], v[198:201], v[190:193], v[78:81]
	v_mfma_f32_16x16x32_bf16 v[132:135], v[202:205], v[164:167], v[132:135]
	v_mfma_f32_16x16x32_bf16 v[74:77], v[202:205], v[190:193], v[74:77]
	v_mfma_f32_16x16x32_bf16 v[128:131], v[206:209], v[164:167], v[128:131]
	v_mfma_f32_16x16x32_bf16 v[70:73], v[206:209], v[190:193], v[70:73]
	v_mfma_f32_16x16x32_bf16 v[124:127], v[210:213], v[164:167], v[124:127]
	v_mfma_f32_16x16x32_bf16 v[66:69], v[210:213], v[190:193], v[66:69]
	s_lshl_b32 s3, s3, 7
	s_waitcnt vmcnt(7)
	ds_write_b128 v189, v[92:95] offset:32768
	s_waitcnt vmcnt(6)
	ds_write_b128 v181, v[100:103] offset:33792
	s_waitcnt vmcnt(5)
	ds_write_b128 v189, v[104:107] offset:34816
	s_waitcnt vmcnt(4)
	ds_write_b128 v181, v[108:111] offset:35840
	s_addk_i32 s3, 0x180
	s_cmp_eq_u32 s2, 6
	s_cselect_b32 s40, s84, 0
	s_cmp_lg_u32 s40, 0
	s_cselect_b32 s3, 0x80, s3
	buffer_load_dwordx4 v[104:107], v182, s[4:7], s3 offen
	buffer_load_dwordx4 v[92:95], v183, s[4:7], s3 offen
	buffer_load_dwordx4 v[112:115], v184, s[4:7], s3 offen
	buffer_load_dwordx4 v[116:119], v185, s[4:7], s3 offen
	s_cmp_gt_u32 s2, 5
	s_cbranch_scc0 .Lmoe_l_b
